# route pass 2: the last read of the residual rows uses nt loads
# baseline (speedup 1.0000x reference)
.LBB0_1884:
	v_and_b32_e32 v62, 0xffffff00, v103
	v_lshl_add_u32 v63, v254, 2, v62
	v_lshlrev_b32_e32 v63, 2, v63
	global_load_dwordx4 v[200:203], v63, s[62:63]
	global_load_dwordx4 v[204:207], v63, s[34:35]
	global_load_dwordx4 v[208:211], v63, s[36:37]
	v_lshlrev_b32_e32 v64, 1, v103
	v_mov_b32_e32 v65, 0
	v_mov_b32_e32 v66, v103
	v_mov_b32_e32 v67, 0
	v_lshl_add_u64 v[196:197], v[48:49], 0, v[64:65]
	v_lshlrev_b32_e32 v68, 6, v62
	v_lshl_add_u32 v68, v254, 4, v68
	v_lshlrev_b32_e32 v69, 12, v75
	v_sub_u32_e32 v68, v68, v69
	v_ashrrev_i32_e32 v69, 31, v68
	v_lshl_add_u64 v[34:35], v[34:35], 0, v[68:69]
	v_lshl_add_u64 v[36:37], v[36:37], 0, v[68:69]
	v_lshl_add_u64 v[38:39], v[38:39], 0, v[68:69]
	v_lshl_add_u64 v[40:41], v[40:41], 0, v[68:69]
	v_mov_b32_e32 v198, 0x1000
	v_mov_b32_e32 v199, 0
	v_lshl_add_u64 v[72:73], v[50:51], 0, v[66:67]
	global_load_dwordx4 v[112:115], v[196:197], off nt
	global_load_dwordx4 v[116:119], v[34:35], off
	global_load_dwordx4 v[120:123], v[36:37], off
	global_load_dwordx4 v[124:127], v[38:39], off
	global_load_dwordx4 v[128:131], v[40:41], off
	global_load_dwordx4 v[132:135], v[196:197], off offset:32 nt
	global_load_dwordx4 v[136:139], v[34:35], off offset:1024
	global_load_dwordx4 v[140:143], v[36:37], off offset:1024
	global_load_dwordx4 v[144:147], v[38:39], off offset:1024
	global_load_dwordx4 v[148:151], v[40:41], off offset:1024
	global_load_dwordx4 v[152:155], v[196:197], off offset:64 nt
	global_load_dwordx4 v[156:159], v[34:35], off offset:2048
	global_load_dwordx4 v[160:163], v[36:37], off offset:2048
	global_load_dwordx4 v[164:167], v[38:39], off offset:2048
	global_load_dwordx4 v[168:171], v[40:41], off offset:2048
	global_load_dwordx4 v[172:175], v[196:197], off offset:96 nt
	global_load_dwordx4 v[176:179], v[34:35], off offset:3072
	global_load_dwordx4 v[180:183], v[36:37], off offset:3072
	global_load_dwordx4 v[184:187], v[38:39], off offset:3072
	global_load_dwordx4 v[188:191], v[40:41], off offset:3072
	v_mul_u32_u24_e32 v62, 12, v62
	v_add_u32_e32 v62, 0x12000, v62
	v_lshl_add_u32 v1, v254, 4, v62
	v_and_b32_e32 v63, 8, v103
	v_lshl_add_u32 v111, v63, 2, v62
	s_waitcnt vmcnt(20)
	v_pk_add_f32 v[204:205], v[204:205], 1.0 op_sel_hi:[1,0]
	v_pk_add_f32 v[206:207], v[206:207], 1.0 op_sel_hi:[1,0]
	ds_write_b128 v1, v[200:203]
	ds_write_b128 v1, v[204:207] offset:1024
	ds_write_b128 v1, v[208:211] offset:2048
	s_waitcnt lgkmcnt(0)
	ds_read_b128 v[200:203], v111 offset:0
	ds_read_b128 v[204:207], v111 offset:16
	ds_read_b128 v[208:211], v111 offset:1024
	ds_read_b128 v[212:215], v111 offset:1040
	ds_read_b128 v[216:219], v111 offset:2048
	ds_read_b128 v[220:223], v111 offset:2064
	s_waitcnt lgkmcnt(0)
	ds_read_b128 v[224:227], v111 offset:64
	ds_read_b128 v[228:231], v111 offset:80
	ds_read_b128 v[232:235], v111 offset:1088
	ds_read_b128 v[236:239], v111 offset:1104
	ds_read_b128 v[240:243], v111 offset:2112
	ds_read_b128 v[244:247], v111 offset:2128
	s_waitcnt vmcnt(15)
	v_lshlrev_b32_e32 v54, 16, v112
	v_and_b32_e32 v55, 0xffff0000, v112
	v_lshlrev_b32_e32 v56, 16, v113
	v_and_b32_e32 v57, 0xffff0000, v113
	v_lshlrev_b32_e32 v58, 16, v114
	v_and_b32_e32 v59, 0xffff0000, v114
	v_lshlrev_b32_e32 v60, 16, v115
	v_and_b32_e32 v61, 0xffff0000, v115
	v_pk_mul_f32 v[54:55], v[46:47], v[54:55]
	v_pk_mul_f32 v[56:57], v[46:47], v[56:57]
	v_pk_mul_f32 v[58:59], v[46:47], v[58:59]
	v_pk_mul_f32 v[60:61], v[46:47], v[60:61]
	v_pk_mul_f32 v[54:55], v[200:201], v[54:55]
	v_pk_mul_f32 v[56:57], v[202:203], v[56:57]
	v_pk_mul_f32 v[58:59], v[204:205], v[58:59]
	v_pk_mul_f32 v[60:61], v[206:207], v[60:61]
	v_pk_fma_f32 v[54:55], v[208:209], v[54:55], v[216:217]
	v_pk_fma_f32 v[56:57], v[210:211], v[56:57], v[218:219]
	v_pk_fma_f32 v[58:59], v[212:213], v[58:59], v[220:221]
	v_pk_fma_f32 v[60:61], v[214:215], v[60:61], v[222:223]
	v_med3_f32 v62, v54, s82, v108
	v_med3_f32 v63, v55, s82, v108
	v_med3_f32 v64, v56, s82, v108
	v_med3_f32 v65, v57, s82, v108
	v_med3_f32 v66, v58, s82, v108
	v_med3_f32 v67, v59, s82, v108
	v_med3_f32 v68, v60, s82, v108
	v_med3_f32 v69, v61, s82, v108
	v_cvt_pk_bf16_f32 v192, v54, v55
	v_cvt_pk_bf16_f32 v193, v56, v57
	v_cvt_pk_bf16_f32 v194, v58, v59
	v_cvt_pk_bf16_f32 v195, v60, v61
	v_cvt_pk_fp8_f32 v70, v62, v63
	v_cvt_pk_fp8_f32 v71, v66, v67
	v_cvt_pk_fp8_f32 v70, v64, v65 op_sel:[0,0,1]
	v_cvt_pk_fp8_f32 v71, v68, v69 op_sel:[0,0,1]
	s_nop 0
	global_store_dwordx2 v[72:73], v[70:71], off
	v_mfma_f32_32x32x16_bf16 v[2:17], v[192:195], v[116:119], v[2:17]
	v_mfma_f32_32x32x16_bf16 v[18:33], v[192:195], v[120:123], v[18:33]
	v_mfma_f32_32x32x16_bf16 v[2:17], v[192:195], v[124:127], v[2:17]
	v_mfma_f32_32x32x16_bf16 v[18:33], v[192:195], v[128:131], v[18:33]
	v_lshlrev_b32_e32 v252, 16, v192
	v_and_b32_e32 v253, 0xffff0000, v192
	v_sub_f32_e32 v62, v54, v252
	v_sub_f32_e32 v63, v55, v253
	v_lshlrev_b32_e32 v252, 16, v193
	v_and_b32_e32 v253, 0xffff0000, v193
	v_sub_f32_e32 v64, v56, v252
	v_sub_f32_e32 v65, v57, v253
	v_lshlrev_b32_e32 v252, 16, v194
	v_and_b32_e32 v253, 0xffff0000, v194
	v_sub_f32_e32 v66, v58, v252
	v_sub_f32_e32 v67, v59, v253
	v_lshlrev_b32_e32 v252, 16, v195
	v_and_b32_e32 v253, 0xffff0000, v195
	v_sub_f32_e32 v68, v60, v252
	v_sub_f32_e32 v69, v61, v253
	v_cvt_pk_bf16_f32 v248, v62, v63
	v_cvt_pk_bf16_f32 v249, v64, v65
	v_cvt_pk_bf16_f32 v250, v66, v67
	v_cvt_pk_bf16_f32 v251, v68, v69
	s_nop 1
	v_mfma_f32_32x32x16_bf16 v[2:17], v[248:251], v[116:119], v[2:17]
	v_mfma_f32_32x32x16_bf16 v[18:33], v[248:251], v[120:123], v[18:33]
	global_load_dwordx4 v[112:115], v[196:197], off offset:128 nt
	v_lshl_add_u64 v[34:35], v[34:35], 0, v[198:199]
	v_lshl_add_u64 v[36:37], v[36:37], 0, v[198:199]
	v_lshl_add_u64 v[38:39], v[38:39], 0, v[198:199]
	v_lshl_add_u64 v[40:41], v[40:41], 0, v[198:199]
	global_load_dwordx4 v[116:119], v[34:35], off
	global_load_dwordx4 v[120:123], v[36:37], off
	global_load_dwordx4 v[124:127], v[38:39], off
	global_load_dwordx4 v[128:131], v[40:41], off
	s_waitcnt lgkmcnt(0)
	ds_read_b128 v[200:203], v111 offset:128
	ds_read_b128 v[204:207], v111 offset:144
	ds_read_b128 v[208:211], v111 offset:1152
	ds_read_b128 v[212:215], v111 offset:1168
	ds_read_b128 v[216:219], v111 offset:2176
	ds_read_b128 v[220:223], v111 offset:2192
	s_waitcnt vmcnt(16)
	v_lshlrev_b32_e32 v54, 16, v132
	v_and_b32_e32 v55, 0xffff0000, v132
	v_lshlrev_b32_e32 v56, 16, v133
	v_and_b32_e32 v57, 0xffff0000, v133
	v_lshlrev_b32_e32 v58, 16, v134
	v_and_b32_e32 v59, 0xffff0000, v134
	v_lshlrev_b32_e32 v60, 16, v135
	v_and_b32_e32 v61, 0xffff0000, v135
	v_pk_mul_f32 v[54:55], v[46:47], v[54:55]
	v_pk_mul_f32 v[56:57], v[46:47], v[56:57]
	v_pk_mul_f32 v[58:59], v[46:47], v[58:59]
	v_pk_mul_f32 v[60:61], v[46:47], v[60:61]
	v_pk_mul_f32 v[54:55], v[224:225], v[54:55]
	v_pk_mul_f32 v[56:57], v[226:227], v[56:57]
	v_pk_mul_f32 v[58:59], v[228:229], v[58:59]
	v_pk_mul_f32 v[60:61], v[230:231], v[60:61]
	v_pk_fma_f32 v[54:55], v[232:233], v[54:55], v[240:241]
	v_pk_fma_f32 v[56:57], v[234:235], v[56:57], v[242:243]
	v_pk_fma_f32 v[58:59], v[236:237], v[58:59], v[244:245]
	v_pk_fma_f32 v[60:61], v[238:239], v[60:61], v[246:247]
	v_med3_f32 v62, v54, s82, v108
	v_med3_f32 v63, v55, s82, v108
	v_med3_f32 v64, v56, s82, v108
	v_med3_f32 v65, v57, s82, v108
	v_med3_f32 v66, v58, s82, v108
	v_med3_f32 v67, v59, s82, v108
	v_med3_f32 v68, v60, s82, v108
	v_med3_f32 v69, v61, s82, v108
	v_cvt_pk_bf16_f32 v192, v54, v55
	v_cvt_pk_bf16_f32 v193, v56, v57
	v_cvt_pk_bf16_f32 v194, v58, v59
	v_cvt_pk_bf16_f32 v195, v60, v61
	v_cvt_pk_fp8_f32 v70, v62, v63
	v_cvt_pk_fp8_f32 v71, v66, v67
	v_cvt_pk_fp8_f32 v70, v64, v65 op_sel:[0,0,1]
	v_cvt_pk_fp8_f32 v71, v68, v69 op_sel:[0,0,1]
	s_nop 0
	global_store_dwordx2 v[72:73], v[70:71], off offset:16
	v_mfma_f32_32x32x16_bf16 v[2:17], v[192:195], v[136:139], v[2:17]
	v_mfma_f32_32x32x16_bf16 v[18:33], v[192:195], v[140:143], v[18:33]
	v_mfma_f32_32x32x16_bf16 v[2:17], v[192:195], v[144:147], v[2:17]
	v_mfma_f32_32x32x16_bf16 v[18:33], v[192:195], v[148:151], v[18:33]
	v_lshlrev_b32_e32 v252, 16, v192
	v_and_b32_e32 v253, 0xffff0000, v192
	v_sub_f32_e32 v62, v54, v252
	v_sub_f32_e32 v63, v55, v253
	v_lshlrev_b32_e32 v252, 16, v193
	v_and_b32_e32 v253, 0xffff0000, v193
	v_sub_f32_e32 v64, v56, v252
	v_sub_f32_e32 v65, v57, v253
	v_lshlrev_b32_e32 v252, 16, v194
	v_and_b32_e32 v253, 0xffff0000, v194
	v_sub_f32_e32 v66, v58, v252
	v_sub_f32_e32 v67, v59, v253
	v_lshlrev_b32_e32 v252, 16, v195
	v_and_b32_e32 v253, 0xffff0000, v195
	v_sub_f32_e32 v68, v60, v252
	v_sub_f32_e32 v69, v61, v253
	v_cvt_pk_bf16_f32 v248, v62, v63
	v_cvt_pk_bf16_f32 v249, v64, v65
	v_cvt_pk_bf16_f32 v250, v66, v67
	v_cvt_pk_bf16_f32 v251, v68, v69
	s_nop 1
	v_mfma_f32_32x32x16_bf16 v[2:17], v[248:251], v[136:139], v[2:17]
	v_mfma_f32_32x32x16_bf16 v[18:33], v[248:251], v[140:143], v[18:33]
	global_load_dwordx4 v[132:135], v[196:197], off offset:160 nt
	global_load_dwordx4 v[136:139], v[34:35], off offset:1024
	global_load_dwordx4 v[140:143], v[36:37], off offset:1024
	global_load_dwordx4 v[144:147], v[38:39], off offset:1024
	global_load_dwordx4 v[148:151], v[40:41], off offset:1024
	s_waitcnt lgkmcnt(0)
	ds_read_b128 v[224:227], v111 offset:192
	ds_read_b128 v[228:231], v111 offset:208
	ds_read_b128 v[232:235], v111 offset:1216
	ds_read_b128 v[236:239], v111 offset:1232
	ds_read_b128 v[240:243], v111 offset:2240
	ds_read_b128 v[244:247], v111 offset:2256
	s_waitcnt vmcnt(17)
	v_lshlrev_b32_e32 v54, 16, v152
	v_and_b32_e32 v55, 0xffff0000, v152
	v_lshlrev_b32_e32 v56, 16, v153
	v_and_b32_e32 v57, 0xffff0000, v153
	v_lshlrev_b32_e32 v58, 16, v154
	v_and_b32_e32 v59, 0xffff0000, v154
	v_lshlrev_b32_e32 v60, 16, v155
	v_and_b32_e32 v61, 0xffff0000, v155
	v_pk_mul_f32 v[54:55], v[46:47], v[54:55]
	v_pk_mul_f32 v[56:57], v[46:47], v[56:57]
	v_pk_mul_f32 v[58:59], v[46:47], v[58:59]
	v_pk_mul_f32 v[60:61], v[46:47], v[60:61]
	v_pk_mul_f32 v[54:55], v[200:201], v[54:55]
	v_pk_mul_f32 v[56:57], v[202:203], v[56:57]
	v_pk_mul_f32 v[58:59], v[204:205], v[58:59]
	v_pk_mul_f32 v[60:61], v[206:207], v[60:61]
	v_pk_fma_f32 v[54:55], v[208:209], v[54:55], v[216:217]
	v_pk_fma_f32 v[56:57], v[210:211], v[56:57], v[218:219]
	v_pk_fma_f32 v[58:59], v[212:213], v[58:59], v[220:221]
	v_pk_fma_f32 v[60:61], v[214:215], v[60:61], v[222:223]
	v_med3_f32 v62, v54, s82, v108
	v_med3_f32 v63, v55, s82, v108
	v_med3_f32 v64, v56, s82, v108
	v_med3_f32 v65, v57, s82, v108
	v_med3_f32 v66, v58, s82, v108
	v_med3_f32 v67, v59, s82, v108
	v_med3_f32 v68, v60, s82, v108
	v_med3_f32 v69, v61, s82, v108
	v_cvt_pk_bf16_f32 v192, v54, v55
	v_cvt_pk_bf16_f32 v193, v56, v57
	v_cvt_pk_bf16_f32 v194, v58, v59
	v_cvt_pk_bf16_f32 v195, v60, v61
	v_cvt_pk_fp8_f32 v70, v62, v63
	v_cvt_pk_fp8_f32 v71, v66, v67
	v_cvt_pk_fp8_f32 v70, v64, v65 op_sel:[0,0,1]
	v_cvt_pk_fp8_f32 v71, v68, v69 op_sel:[0,0,1]
	s_nop 0
	global_store_dwordx2 v[72:73], v[70:71], off offset:32
	v_mfma_f32_32x32x16_bf16 v[2:17], v[192:195], v[156:159], v[2:17]
	v_mfma_f32_32x32x16_bf16 v[18:33], v[192:195], v[160:163], v[18:33]
	v_mfma_f32_32x32x16_bf16 v[2:17], v[192:195], v[164:167], v[2:17]
	v_mfma_f32_32x32x16_bf16 v[18:33], v[192:195], v[168:171], v[18:33]
	v_lshlrev_b32_e32 v252, 16, v192
	v_and_b32_e32 v253, 0xffff0000, v192
	v_sub_f32_e32 v62, v54, v252
	v_sub_f32_e32 v63, v55, v253
	v_lshlrev_b32_e32 v252, 16, v193
	v_and_b32_e32 v253, 0xffff0000, v193
	v_sub_f32_e32 v64, v56, v252
	v_sub_f32_e32 v65, v57, v253
	v_lshlrev_b32_e32 v252, 16, v194
	v_and_b32_e32 v253, 0xffff0000, v194
	v_sub_f32_e32 v66, v58, v252
	v_sub_f32_e32 v67, v59, v253
	v_lshlrev_b32_e32 v252, 16, v195
	v_and_b32_e32 v253, 0xffff0000, v195
	v_sub_f32_e32 v68, v60, v252
	v_sub_f32_e32 v69, v61, v253
	v_cvt_pk_bf16_f32 v248, v62, v63
	v_cvt_pk_bf16_f32 v249, v64, v65
	v_cvt_pk_bf16_f32 v250, v66, v67
	v_cvt_pk_bf16_f32 v251, v68, v69
	s_nop 1
	v_mfma_f32_32x32x16_bf16 v[2:17], v[248:251], v[156:159], v[2:17]
	v_mfma_f32_32x32x16_bf16 v[18:33], v[248:251], v[160:163], v[18:33]
	global_load_dwordx4 v[152:155], v[196:197], off offset:192 nt
	global_load_dwordx4 v[156:159], v[34:35], off offset:2048
	global_load_dwordx4 v[160:163], v[36:37], off offset:2048
	global_load_dwordx4 v[164:167], v[38:39], off offset:2048
	global_load_dwordx4 v[168:171], v[40:41], off offset:2048
	s_waitcnt lgkmcnt(0)
	ds_read_b128 v[200:203], v111 offset:256
	ds_read_b128 v[204:207], v111 offset:272
	ds_read_b128 v[208:211], v111 offset:1280
	ds_read_b128 v[212:215], v111 offset:1296
	ds_read_b128 v[216:219], v111 offset:2304
	ds_read_b128 v[220:223], v111 offset:2320
	s_waitcnt vmcnt(18)
	v_lshlrev_b32_e32 v54, 16, v172
	v_and_b32_e32 v55, 0xffff0000, v172
	v_lshlrev_b32_e32 v56, 16, v173
	v_and_b32_e32 v57, 0xffff0000, v173
	v_lshlrev_b32_e32 v58, 16, v174
	v_and_b32_e32 v59, 0xffff0000, v174
	v_lshlrev_b32_e32 v60, 16, v175
	v_and_b32_e32 v61, 0xffff0000, v175
	v_pk_mul_f32 v[54:55], v[46:47], v[54:55]
	v_pk_mul_f32 v[56:57], v[46:47], v[56:57]
	v_pk_mul_f32 v[58:59], v[46:47], v[58:59]
	v_pk_mul_f32 v[60:61], v[46:47], v[60:61]
	v_pk_mul_f32 v[54:55], v[224:225], v[54:55]
	v_pk_mul_f32 v[56:57], v[226:227], v[56:57]
	v_pk_mul_f32 v[58:59], v[228:229], v[58:59]
	v_pk_mul_f32 v[60:61], v[230:231], v[60:61]
	v_pk_fma_f32 v[54:55], v[232:233], v[54:55], v[240:241]
	v_pk_fma_f32 v[56:57], v[234:235], v[56:57], v[242:243]
	v_pk_fma_f32 v[58:59], v[236:237], v[58:59], v[244:245]
	v_pk_fma_f32 v[60:61], v[238:239], v[60:61], v[246:247]
	v_med3_f32 v62, v54, s82, v108
	v_med3_f32 v63, v55, s82, v108
	v_med3_f32 v64, v56, s82, v108
	v_med3_f32 v65, v57, s82, v108
	v_med3_f32 v66, v58, s82, v108
	v_med3_f32 v67, v59, s82, v108
	v_med3_f32 v68, v60, s82, v108
	v_med3_f32 v69, v61, s82, v108
	v_cvt_pk_bf16_f32 v192, v54, v55
	v_cvt_pk_bf16_f32 v193, v56, v57
	v_cvt_pk_bf16_f32 v194, v58, v59
	v_cvt_pk_bf16_f32 v195, v60, v61
	v_cvt_pk_fp8_f32 v70, v62, v63
	v_cvt_pk_fp8_f32 v71, v66, v67
	v_cvt_pk_fp8_f32 v70, v64, v65 op_sel:[0,0,1]
	v_cvt_pk_fp8_f32 v71, v68, v69 op_sel:[0,0,1]
	s_nop 0
	global_store_dwordx2 v[72:73], v[70:71], off offset:48
	v_mfma_f32_32x32x16_bf16 v[2:17], v[192:195], v[176:179], v[2:17]
	v_mfma_f32_32x32x16_bf16 v[18:33], v[192:195], v[180:183], v[18:33]
	v_mfma_f32_32x32x16_bf16 v[2:17], v[192:195], v[184:187], v[2:17]
	v_mfma_f32_32x32x16_bf16 v[18:33], v[192:195], v[188:191], v[18:33]
	v_lshlrev_b32_e32 v252, 16, v192
	v_and_b32_e32 v253, 0xffff0000, v192
	v_sub_f32_e32 v62, v54, v252
	v_sub_f32_e32 v63, v55, v253
	v_lshlrev_b32_e32 v252, 16, v193
	v_and_b32_e32 v253, 0xffff0000, v193
	v_sub_f32_e32 v64, v56, v252
	v_sub_f32_e32 v65, v57, v253
	v_lshlrev_b32_e32 v252, 16, v194
	v_and_b32_e32 v253, 0xffff0000, v194
	v_sub_f32_e32 v66, v58, v252
	v_sub_f32_e32 v67, v59, v253
	v_lshlrev_b32_e32 v252, 16, v195
	v_and_b32_e32 v253, 0xffff0000, v195
	v_sub_f32_e32 v68, v60, v252
	v_sub_f32_e32 v69, v61, v253
	v_cvt_pk_bf16_f32 v248, v62, v63
	v_cvt_pk_bf16_f32 v249, v64, v65
	v_cvt_pk_bf16_f32 v250, v66, v67
	v_cvt_pk_bf16_f32 v251, v68, v69
	s_nop 1
	v_mfma_f32_32x32x16_bf16 v[2:17], v[248:251], v[176:179], v[2:17]
	v_mfma_f32_32x32x16_bf16 v[18:33], v[248:251], v[180:183], v[18:33]
	global_load_dwordx4 v[172:175], v[196:197], off offset:224 nt
	global_load_dwordx4 v[176:179], v[34:35], off offset:3072
	global_load_dwordx4 v[180:183], v[36:37], off offset:3072
	global_load_dwordx4 v[184:187], v[38:39], off offset:3072
	global_load_dwordx4 v[188:191], v[40:41], off offset:3072
	s_waitcnt lgkmcnt(0)
	ds_read_b128 v[224:227], v111 offset:320
	ds_read_b128 v[228:231], v111 offset:336
	ds_read_b128 v[232:235], v111 offset:1344
	ds_read_b128 v[236:239], v111 offset:1360
	ds_read_b128 v[240:243], v111 offset:2368
	ds_read_b128 v[244:247], v111 offset:2384
	s_waitcnt vmcnt(18)
	v_lshlrev_b32_e32 v54, 16, v112
	v_and_b32_e32 v55, 0xffff0000, v112
	v_lshlrev_b32_e32 v56, 16, v113
	v_and_b32_e32 v57, 0xffff0000, v113
	v_lshlrev_b32_e32 v58, 16, v114
	v_and_b32_e32 v59, 0xffff0000, v114
	v_lshlrev_b32_e32 v60, 16, v115
	v_and_b32_e32 v61, 0xffff0000, v115
	v_pk_mul_f32 v[54:55], v[46:47], v[54:55]
	v_pk_mul_f32 v[56:57], v[46:47], v[56:57]
	v_pk_mul_f32 v[58:59], v[46:47], v[58:59]
	v_pk_mul_f32 v[60:61], v[46:47], v[60:61]
	v_pk_mul_f32 v[54:55], v[200:201], v[54:55]
	v_pk_mul_f32 v[56:57], v[202:203], v[56:57]
	v_pk_mul_f32 v[58:59], v[204:205], v[58:59]
	v_pk_mul_f32 v[60:61], v[206:207], v[60:61]
	v_pk_fma_f32 v[54:55], v[208:209], v[54:55], v[216:217]
	v_pk_fma_f32 v[56:57], v[210:211], v[56:57], v[218:219]
	v_pk_fma_f32 v[58:59], v[212:213], v[58:59], v[220:221]
	v_pk_fma_f32 v[60:61], v[214:215], v[60:61], v[222:223]
	v_med3_f32 v62, v54, s82, v108
	v_med3_f32 v63, v55, s82, v108
	v_med3_f32 v64, v56, s82, v108
	v_med3_f32 v65, v57, s82, v108
	v_med3_f32 v66, v58, s82, v108
	v_med3_f32 v67, v59, s82, v108
	v_med3_f32 v68, v60, s82, v108
	v_med3_f32 v69, v61, s82, v108
	v_cvt_pk_bf16_f32 v192, v54, v55
	v_cvt_pk_bf16_f32 v193, v56, v57
	v_cvt_pk_bf16_f32 v194, v58, v59
	v_cvt_pk_bf16_f32 v195, v60, v61
	v_cvt_pk_fp8_f32 v70, v62, v63
	v_cvt_pk_fp8_f32 v71, v66, v67
	v_cvt_pk_fp8_f32 v70, v64, v65 op_sel:[0,0,1]
	v_cvt_pk_fp8_f32 v71, v68, v69 op_sel:[0,0,1]
	s_nop 0
	global_store_dwordx2 v[72:73], v[70:71], off offset:64
	v_mfma_f32_32x32x16_bf16 v[2:17], v[192:195], v[116:119], v[2:17]
	v_mfma_f32_32x32x16_bf16 v[18:33], v[192:195], v[120:123], v[18:33]
	v_mfma_f32_32x32x16_bf16 v[2:17], v[192:195], v[124:127], v[2:17]
	v_mfma_f32_32x32x16_bf16 v[18:33], v[192:195], v[128:131], v[18:33]
	v_lshlrev_b32_e32 v252, 16, v192
	v_and_b32_e32 v253, 0xffff0000, v192
	v_sub_f32_e32 v62, v54, v252
	v_sub_f32_e32 v63, v55, v253
	v_lshlrev_b32_e32 v252, 16, v193
	v_and_b32_e32 v253, 0xffff0000, v193
	v_sub_f32_e32 v64, v56, v252
	v_sub_f32_e32 v65, v57, v253
	v_lshlrev_b32_e32 v252, 16, v194
	v_and_b32_e32 v253, 0xffff0000, v194
	v_sub_f32_e32 v66, v58, v252
	v_sub_f32_e32 v67, v59, v253
	v_lshlrev_b32_e32 v252, 16, v195
	v_and_b32_e32 v253, 0xffff0000, v195
	v_sub_f32_e32 v68, v60, v252
	v_sub_f32_e32 v69, v61, v253
	v_cvt_pk_bf16_f32 v248, v62, v63
	v_cvt_pk_bf16_f32 v249, v64, v65
	v_cvt_pk_bf16_f32 v250, v66, v67
	v_cvt_pk_bf16_f32 v251, v68, v69
	s_nop 1
	v_mfma_f32_32x32x16_bf16 v[2:17], v[248:251], v[116:119], v[2:17]
	v_mfma_f32_32x32x16_bf16 v[18:33], v[248:251], v[120:123], v[18:33]
	global_load_dwordx4 v[112:115], v[196:197], off offset:256 nt
	v_lshl_add_u64 v[34:35], v[34:35], 0, v[198:199]
	v_lshl_add_u64 v[36:37], v[36:37], 0, v[198:199]
	v_lshl_add_u64 v[38:39], v[38:39], 0, v[198:199]
	v_lshl_add_u64 v[40:41], v[40:41], 0, v[198:199]
	global_load_dwordx4 v[116:119], v[34:35], off
	global_load_dwordx4 v[120:123], v[36:37], off
	global_load_dwordx4 v[124:127], v[38:39], off
	global_load_dwordx4 v[128:131], v[40:41], off
	s_waitcnt lgkmcnt(0)
	ds_read_b128 v[200:203], v111 offset:384
	ds_read_b128 v[204:207], v111 offset:400
	ds_read_b128 v[208:211], v111 offset:1408
	ds_read_b128 v[212:215], v111 offset:1424
	ds_read_b128 v[216:219], v111 offset:2432
	ds_read_b128 v[220:223], v111 offset:2448
	s_waitcnt vmcnt(18)
	v_lshlrev_b32_e32 v54, 16, v132
	v_and_b32_e32 v55, 0xffff0000, v132
	v_lshlrev_b32_e32 v56, 16, v133
	v_and_b32_e32 v57, 0xffff0000, v133
	v_lshlrev_b32_e32 v58, 16, v134
	v_and_b32_e32 v59, 0xffff0000, v134
	v_lshlrev_b32_e32 v60, 16, v135
	v_and_b32_e32 v61, 0xffff0000, v135
	v_pk_mul_f32 v[54:55], v[46:47], v[54:55]
	v_pk_mul_f32 v[56:57], v[46:47], v[56:57]
	v_pk_mul_f32 v[58:59], v[46:47], v[58:59]
	v_pk_mul_f32 v[60:61], v[46:47], v[60:61]
	v_pk_mul_f32 v[54:55], v[224:225], v[54:55]
	v_pk_mul_f32 v[56:57], v[226:227], v[56:57]
	v_pk_mul_f32 v[58:59], v[228:229], v[58:59]
	v_pk_mul_f32 v[60:61], v[230:231], v[60:61]
	v_pk_fma_f32 v[54:55], v[232:233], v[54:55], v[240:241]
	v_pk_fma_f32 v[56:57], v[234:235], v[56:57], v[242:243]
	v_pk_fma_f32 v[58:59], v[236:237], v[58:59], v[244:245]
	v_pk_fma_f32 v[60:61], v[238:239], v[60:61], v[246:247]
	v_med3_f32 v62, v54, s82, v108
	v_med3_f32 v63, v55, s82, v108
	v_med3_f32 v64, v56, s82, v108
	v_med3_f32 v65, v57, s82, v108
	v_med3_f32 v66, v58, s82, v108
	v_med3_f32 v67, v59, s82, v108
	v_med3_f32 v68, v60, s82, v108
	v_med3_f32 v69, v61, s82, v108
	v_cvt_pk_bf16_f32 v192, v54, v55
	v_cvt_pk_bf16_f32 v193, v56, v57
	v_cvt_pk_bf16_f32 v194, v58, v59
	v_cvt_pk_bf16_f32 v195, v60, v61
	v_cvt_pk_fp8_f32 v70, v62, v63
	v_cvt_pk_fp8_f32 v71, v66, v67
	v_cvt_pk_fp8_f32 v70, v64, v65 op_sel:[0,0,1]
	v_cvt_pk_fp8_f32 v71, v68, v69 op_sel:[0,0,1]
	s_nop 0
	global_store_dwordx2 v[72:73], v[70:71], off offset:80
	v_mfma_f32_32x32x16_bf16 v[2:17], v[192:195], v[136:139], v[2:17]
	v_mfma_f32_32x32x16_bf16 v[18:33], v[192:195], v[140:143], v[18:33]
	v_mfma_f32_32x32x16_bf16 v[2:17], v[192:195], v[144:147], v[2:17]
	v_mfma_f32_32x32x16_bf16 v[18:33], v[192:195], v[148:151], v[18:33]
	v_lshlrev_b32_e32 v252, 16, v192
	v_and_b32_e32 v253, 0xffff0000, v192
	v_sub_f32_e32 v62, v54, v252
	v_sub_f32_e32 v63, v55, v253
	v_lshlrev_b32_e32 v252, 16, v193
	v_and_b32_e32 v253, 0xffff0000, v193
	v_sub_f32_e32 v64, v56, v252
	v_sub_f32_e32 v65, v57, v253
	v_lshlrev_b32_e32 v252, 16, v194
	v_and_b32_e32 v253, 0xffff0000, v194
	v_sub_f32_e32 v66, v58, v252
	v_sub_f32_e32 v67, v59, v253
	v_lshlrev_b32_e32 v252, 16, v195
	v_and_b32_e32 v253, 0xffff0000, v195
	v_sub_f32_e32 v68, v60, v252
	v_sub_f32_e32 v69, v61, v253
	v_cvt_pk_bf16_f32 v248, v62, v63
	v_cvt_pk_bf16_f32 v249, v64, v65
	v_cvt_pk_bf16_f32 v250, v66, v67
	v_cvt_pk_bf16_f32 v251, v68, v69
	s_nop 1
	v_mfma_f32_32x32x16_bf16 v[2:17], v[248:251], v[136:139], v[2:17]
	v_mfma_f32_32x32x16_bf16 v[18:33], v[248:251], v[140:143], v[18:33]
	global_load_dwordx4 v[132:135], v[196:197], off offset:288 nt
	global_load_dwordx4 v[136:139], v[34:35], off offset:1024
	global_load_dwordx4 v[140:143], v[36:37], off offset:1024
	global_load_dwordx4 v[144:147], v[38:39], off offset:1024
	global_load_dwordx4 v[148:151], v[40:41], off offset:1024
	s_waitcnt lgkmcnt(0)
	ds_read_b128 v[224:227], v111 offset:448
	ds_read_b128 v[228:231], v111 offset:464
	ds_read_b128 v[232:235], v111 offset:1472
	ds_read_b128 v[236:239], v111 offset:1488
	ds_read_b128 v[240:243], v111 offset:2496
	ds_read_b128 v[244:247], v111 offset:2512
	s_waitcnt vmcnt(18)
	v_lshlrev_b32_e32 v54, 16, v152
	v_and_b32_e32 v55, 0xffff0000, v152
	v_lshlrev_b32_e32 v56, 16, v153
	v_and_b32_e32 v57, 0xffff0000, v153
	v_lshlrev_b32_e32 v58, 16, v154
	v_and_b32_e32 v59, 0xffff0000, v154
	v_lshlrev_b32_e32 v60, 16, v155
	v_and_b32_e32 v61, 0xffff0000, v155
	v_pk_mul_f32 v[54:55], v[46:47], v[54:55]
	v_pk_mul_f32 v[56:57], v[46:47], v[56:57]
	v_pk_mul_f32 v[58:59], v[46:47], v[58:59]
	v_pk_mul_f32 v[60:61], v[46:47], v[60:61]
	v_pk_mul_f32 v[54:55], v[200:201], v[54:55]
	v_pk_mul_f32 v[56:57], v[202:203], v[56:57]
	v_pk_mul_f32 v[58:59], v[204:205], v[58:59]
	v_pk_mul_f32 v[60:61], v[206:207], v[60:61]
	v_pk_fma_f32 v[54:55], v[208:209], v[54:55], v[216:217]
	v_pk_fma_f32 v[56:57], v[210:211], v[56:57], v[218:219]
	v_pk_fma_f32 v[58:59], v[212:213], v[58:59], v[220:221]
	v_pk_fma_f32 v[60:61], v[214:215], v[60:61], v[222:223]
	v_med3_f32 v62, v54, s82, v108
	v_med3_f32 v63, v55, s82, v108
	v_med3_f32 v64, v56, s82, v108
	v_med3_f32 v65, v57, s82, v108
	v_med3_f32 v66, v58, s82, v108
	v_med3_f32 v67, v59, s82, v108
	v_med3_f32 v68, v60, s82, v108
	v_med3_f32 v69, v61, s82, v108
	v_cvt_pk_bf16_f32 v192, v54, v55
	v_cvt_pk_bf16_f32 v193, v56, v57
	v_cvt_pk_bf16_f32 v194, v58, v59
	v_cvt_pk_bf16_f32 v195, v60, v61
	v_cvt_pk_fp8_f32 v70, v62, v63
	v_cvt_pk_fp8_f32 v71, v66, v67
	v_cvt_pk_fp8_f32 v70, v64, v65 op_sel:[0,0,1]
	v_cvt_pk_fp8_f32 v71, v68, v69 op_sel:[0,0,1]
	s_nop 0
	global_store_dwordx2 v[72:73], v[70:71], off offset:96
	v_mfma_f32_32x32x16_bf16 v[2:17], v[192:195], v[156:159], v[2:17]
	v_mfma_f32_32x32x16_bf16 v[18:33], v[192:195], v[160:163], v[18:33]
	v_mfma_f32_32x32x16_bf16 v[2:17], v[192:195], v[164:167], v[2:17]
	v_mfma_f32_32x32x16_bf16 v[18:33], v[192:195], v[168:171], v[18:33]
	v_lshlrev_b32_e32 v252, 16, v192
	v_and_b32_e32 v253, 0xffff0000, v192
	v_sub_f32_e32 v62, v54, v252
	v_sub_f32_e32 v63, v55, v253
	v_lshlrev_b32_e32 v252, 16, v193
	v_and_b32_e32 v253, 0xffff0000, v193
	v_sub_f32_e32 v64, v56, v252
	v_sub_f32_e32 v65, v57, v253
	v_lshlrev_b32_e32 v252, 16, v194
	v_and_b32_e32 v253, 0xffff0000, v194
	v_sub_f32_e32 v66, v58, v252
	v_sub_f32_e32 v67, v59, v253
	v_lshlrev_b32_e32 v252, 16, v195
	v_and_b32_e32 v253, 0xffff0000, v195
	v_sub_f32_e32 v68, v60, v252
	v_sub_f32_e32 v69, v61, v253
	v_cvt_pk_bf16_f32 v248, v62, v63
	v_cvt_pk_bf16_f32 v249, v64, v65
	v_cvt_pk_bf16_f32 v250, v66, v67
	v_cvt_pk_bf16_f32 v251, v68, v69
	s_nop 1
	v_mfma_f32_32x32x16_bf16 v[2:17], v[248:251], v[156:159], v[2:17]
	v_mfma_f32_32x32x16_bf16 v[18:33], v[248:251], v[160:163], v[18:33]
	global_load_dwordx4 v[152:155], v[196:197], off offset:320 nt
	global_load_dwordx4 v[156:159], v[34:35], off offset:2048
	global_load_dwordx4 v[160:163], v[36:37], off offset:2048
	global_load_dwordx4 v[164:167], v[38:39], off offset:2048
	global_load_dwordx4 v[168:171], v[40:41], off offset:2048
	s_waitcnt lgkmcnt(0)
	ds_read_b128 v[200:203], v111 offset:512
	ds_read_b128 v[204:207], v111 offset:528
	ds_read_b128 v[208:211], v111 offset:1536
	ds_read_b128 v[212:215], v111 offset:1552
	ds_read_b128 v[216:219], v111 offset:2560
	ds_read_b128 v[220:223], v111 offset:2576
	s_waitcnt vmcnt(18)
	v_lshlrev_b32_e32 v54, 16, v172
	v_and_b32_e32 v55, 0xffff0000, v172
	v_lshlrev_b32_e32 v56, 16, v173
	v_and_b32_e32 v57, 0xffff0000, v173
	v_lshlrev_b32_e32 v58, 16, v174
	v_and_b32_e32 v59, 0xffff0000, v174
	v_lshlrev_b32_e32 v60, 16, v175
	v_and_b32_e32 v61, 0xffff0000, v175
	v_pk_mul_f32 v[54:55], v[46:47], v[54:55]
	v_pk_mul_f32 v[56:57], v[46:47], v[56:57]
	v_pk_mul_f32 v[58:59], v[46:47], v[58:59]
	v_pk_mul_f32 v[60:61], v[46:47], v[60:61]
	v_pk_mul_f32 v[54:55], v[224:225], v[54:55]
	v_pk_mul_f32 v[56:57], v[226:227], v[56:57]
	v_pk_mul_f32 v[58:59], v[228:229], v[58:59]
	v_pk_mul_f32 v[60:61], v[230:231], v[60:61]
	v_pk_fma_f32 v[54:55], v[232:233], v[54:55], v[240:241]
	v_pk_fma_f32 v[56:57], v[234:235], v[56:57], v[242:243]
	v_pk_fma_f32 v[58:59], v[236:237], v[58:59], v[244:245]
	v_pk_fma_f32 v[60:61], v[238:239], v[60:61], v[246:247]
	v_med3_f32 v62, v54, s82, v108
	v_med3_f32 v63, v55, s82, v108
	v_med3_f32 v64, v56, s82, v108
	v_med3_f32 v65, v57, s82, v108
	v_med3_f32 v66, v58, s82, v108
	v_med3_f32 v67, v59, s82, v108
	v_med3_f32 v68, v60, s82, v108
	v_med3_f32 v69, v61, s82, v108
	v_cvt_pk_bf16_f32 v192, v54, v55
	v_cvt_pk_bf16_f32 v193, v56, v57
	v_cvt_pk_bf16_f32 v194, v58, v59
	v_cvt_pk_bf16_f32 v195, v60, v61
	v_cvt_pk_fp8_f32 v70, v62, v63
	v_cvt_pk_fp8_f32 v71, v66, v67
	v_cvt_pk_fp8_f32 v70, v64, v65 op_sel:[0,0,1]
	v_cvt_pk_fp8_f32 v71, v68, v69 op_sel:[0,0,1]
	s_nop 0
	global_store_dwordx2 v[72:73], v[70:71], off offset:112
	v_mfma_f32_32x32x16_bf16 v[2:17], v[192:195], v[176:179], v[2:17]
	v_mfma_f32_32x32x16_bf16 v[18:33], v[192:195], v[180:183], v[18:33]
	v_mfma_f32_32x32x16_bf16 v[2:17], v[192:195], v[184:187], v[2:17]
	v_mfma_f32_32x32x16_bf16 v[18:33], v[192:195], v[188:191], v[18:33]
	v_lshlrev_b32_e32 v252, 16, v192
	v_and_b32_e32 v253, 0xffff0000, v192
	v_sub_f32_e32 v62, v54, v252
	v_sub_f32_e32 v63, v55, v253
	v_lshlrev_b32_e32 v252, 16, v193
	v_and_b32_e32 v253, 0xffff0000, v193
	v_sub_f32_e32 v64, v56, v252
	v_sub_f32_e32 v65, v57, v253
	v_lshlrev_b32_e32 v252, 16, v194
	v_and_b32_e32 v253, 0xffff0000, v194
	v_sub_f32_e32 v66, v58, v252
	v_sub_f32_e32 v67, v59, v253
	v_lshlrev_b32_e32 v252, 16, v195
	v_and_b32_e32 v253, 0xffff0000, v195
	v_sub_f32_e32 v68, v60, v252
	v_sub_f32_e32 v69, v61, v253
	v_cvt_pk_bf16_f32 v248, v62, v63
	v_cvt_pk_bf16_f32 v249, v64, v65
	v_cvt_pk_bf16_f32 v250, v66, v67
	v_cvt_pk_bf16_f32 v251, v68, v69
	s_nop 1
	v_mfma_f32_32x32x16_bf16 v[2:17], v[248:251], v[176:179], v[2:17]
	v_mfma_f32_32x32x16_bf16 v[18:33], v[248:251], v[180:183], v[18:33]
	global_load_dwordx4 v[172:175], v[196:197], off offset:352 nt
	global_load_dwordx4 v[176:179], v[34:35], off offset:3072
	global_load_dwordx4 v[180:183], v[36:37], off offset:3072
	global_load_dwordx4 v[184:187], v[38:39], off offset:3072
	global_load_dwordx4 v[188:191], v[40:41], off offset:3072
	s_waitcnt lgkmcnt(0)
	ds_read_b128 v[224:227], v111 offset:576
	ds_read_b128 v[228:231], v111 offset:592
	ds_read_b128 v[232:235], v111 offset:1600
	ds_read_b128 v[236:239], v111 offset:1616
	ds_read_b128 v[240:243], v111 offset:2624
	ds_read_b128 v[244:247], v111 offset:2640
	s_waitcnt vmcnt(18)
	v_lshlrev_b32_e32 v54, 16, v112
	v_and_b32_e32 v55, 0xffff0000, v112
	v_lshlrev_b32_e32 v56, 16, v113
	v_and_b32_e32 v57, 0xffff0000, v113
	v_lshlrev_b32_e32 v58, 16, v114
	v_and_b32_e32 v59, 0xffff0000, v114
	v_lshlrev_b32_e32 v60, 16, v115
	v_and_b32_e32 v61, 0xffff0000, v115
	v_pk_mul_f32 v[54:55], v[46:47], v[54:55]
	v_pk_mul_f32 v[56:57], v[46:47], v[56:57]
	v_pk_mul_f32 v[58:59], v[46:47], v[58:59]
	v_pk_mul_f32 v[60:61], v[46:47], v[60:61]
	v_pk_mul_f32 v[54:55], v[200:201], v[54:55]
	v_pk_mul_f32 v[56:57], v[202:203], v[56:57]
	v_pk_mul_f32 v[58:59], v[204:205], v[58:59]
	v_pk_mul_f32 v[60:61], v[206:207], v[60:61]
	v_pk_fma_f32 v[54:55], v[208:209], v[54:55], v[216:217]
	v_pk_fma_f32 v[56:57], v[210:211], v[56:57], v[218:219]
	v_pk_fma_f32 v[58:59], v[212:213], v[58:59], v[220:221]
	v_pk_fma_f32 v[60:61], v[214:215], v[60:61], v[222:223]
	v_med3_f32 v62, v54, s82, v108
	v_med3_f32 v63, v55, s82, v108
	v_med3_f32 v64, v56, s82, v108
	v_med3_f32 v65, v57, s82, v108
	v_med3_f32 v66, v58, s82, v108
	v_med3_f32 v67, v59, s82, v108
	v_med3_f32 v68, v60, s82, v108
	v_med3_f32 v69, v61, s82, v108
	v_cvt_pk_bf16_f32 v192, v54, v55
	v_cvt_pk_bf16_f32 v193, v56, v57
	v_cvt_pk_bf16_f32 v194, v58, v59
	v_cvt_pk_bf16_f32 v195, v60, v61
	v_cvt_pk_fp8_f32 v70, v62, v63
	v_cvt_pk_fp8_f32 v71, v66, v67
	v_cvt_pk_fp8_f32 v70, v64, v65 op_sel:[0,0,1]
	v_cvt_pk_fp8_f32 v71, v68, v69 op_sel:[0,0,1]
	s_nop 0
	global_store_dwordx2 v[72:73], v[70:71], off offset:128
	v_mfma_f32_32x32x16_bf16 v[2:17], v[192:195], v[116:119], v[2:17]
	v_mfma_f32_32x32x16_bf16 v[18:33], v[192:195], v[120:123], v[18:33]
	v_mfma_f32_32x32x16_bf16 v[2:17], v[192:195], v[124:127], v[2:17]
	v_mfma_f32_32x32x16_bf16 v[18:33], v[192:195], v[128:131], v[18:33]
	v_lshlrev_b32_e32 v252, 16, v192
	v_and_b32_e32 v253, 0xffff0000, v192
	v_sub_f32_e32 v62, v54, v252
	v_sub_f32_e32 v63, v55, v253
	v_lshlrev_b32_e32 v252, 16, v193
	v_and_b32_e32 v253, 0xffff0000, v193
	v_sub_f32_e32 v64, v56, v252
	v_sub_f32_e32 v65, v57, v253
	v_lshlrev_b32_e32 v252, 16, v194
	v_and_b32_e32 v253, 0xffff0000, v194
	v_sub_f32_e32 v66, v58, v252
	v_sub_f32_e32 v67, v59, v253
	v_lshlrev_b32_e32 v252, 16, v195
	v_and_b32_e32 v253, 0xffff0000, v195
	v_sub_f32_e32 v68, v60, v252
	v_sub_f32_e32 v69, v61, v253
	v_cvt_pk_bf16_f32 v248, v62, v63
	v_cvt_pk_bf16_f32 v249, v64, v65
	v_cvt_pk_bf16_f32 v250, v66, v67
	v_cvt_pk_bf16_f32 v251, v68, v69
	s_nop 1
	v_mfma_f32_32x32x16_bf16 v[2:17], v[248:251], v[116:119], v[2:17]
	v_mfma_f32_32x32x16_bf16 v[18:33], v[248:251], v[120:123], v[18:33]
	global_load_dwordx4 v[112:115], v[196:197], off offset:384 nt
	v_lshl_add_u64 v[34:35], v[34:35], 0, v[198:199]
	v_lshl_add_u64 v[36:37], v[36:37], 0, v[198:199]
	v_lshl_add_u64 v[38:39], v[38:39], 0, v[198:199]
	v_lshl_add_u64 v[40:41], v[40:41], 0, v[198:199]
	global_load_dwordx4 v[116:119], v[34:35], off
	global_load_dwordx4 v[120:123], v[36:37], off
	global_load_dwordx4 v[124:127], v[38:39], off
	global_load_dwordx4 v[128:131], v[40:41], off
	s_waitcnt lgkmcnt(0)
	ds_read_b128 v[200:203], v111 offset:640
	ds_read_b128 v[204:207], v111 offset:656
	ds_read_b128 v[208:211], v111 offset:1664
	ds_read_b128 v[212:215], v111 offset:1680
	ds_read_b128 v[216:219], v111 offset:2688
	ds_read_b128 v[220:223], v111 offset:2704
	s_waitcnt vmcnt(18)
	v_lshlrev_b32_e32 v54, 16, v132
	v_and_b32_e32 v55, 0xffff0000, v132
	v_lshlrev_b32_e32 v56, 16, v133
	v_and_b32_e32 v57, 0xffff0000, v133
	v_lshlrev_b32_e32 v58, 16, v134
	v_and_b32_e32 v59, 0xffff0000, v134
	v_lshlrev_b32_e32 v60, 16, v135
	v_and_b32_e32 v61, 0xffff0000, v135
	v_pk_mul_f32 v[54:55], v[46:47], v[54:55]
	v_pk_mul_f32 v[56:57], v[46:47], v[56:57]
	v_pk_mul_f32 v[58:59], v[46:47], v[58:59]
	v_pk_mul_f32 v[60:61], v[46:47], v[60:61]
	v_pk_mul_f32 v[54:55], v[224:225], v[54:55]
	v_pk_mul_f32 v[56:57], v[226:227], v[56:57]
	v_pk_mul_f32 v[58:59], v[228:229], v[58:59]
	v_pk_mul_f32 v[60:61], v[230:231], v[60:61]
	v_pk_fma_f32 v[54:55], v[232:233], v[54:55], v[240:241]
	v_pk_fma_f32 v[56:57], v[234:235], v[56:57], v[242:243]
	v_pk_fma_f32 v[58:59], v[236:237], v[58:59], v[244:245]
	v_pk_fma_f32 v[60:61], v[238:239], v[60:61], v[246:247]
	v_med3_f32 v62, v54, s82, v108
	v_med3_f32 v63, v55, s82, v108
	v_med3_f32 v64, v56, s82, v108
	v_med3_f32 v65, v57, s82, v108
	v_med3_f32 v66, v58, s82, v108
	v_med3_f32 v67, v59, s82, v108
	v_med3_f32 v68, v60, s82, v108
	v_med3_f32 v69, v61, s82, v108
	v_cvt_pk_bf16_f32 v192, v54, v55
	v_cvt_pk_bf16_f32 v193, v56, v57
	v_cvt_pk_bf16_f32 v194, v58, v59
	v_cvt_pk_bf16_f32 v195, v60, v61
	v_cvt_pk_fp8_f32 v70, v62, v63
	v_cvt_pk_fp8_f32 v71, v66, v67
	v_cvt_pk_fp8_f32 v70, v64, v65 op_sel:[0,0,1]
	v_cvt_pk_fp8_f32 v71, v68, v69 op_sel:[0,0,1]
	s_nop 0
	global_store_dwordx2 v[72:73], v[70:71], off offset:144
	v_mfma_f32_32x32x16_bf16 v[2:17], v[192:195], v[136:139], v[2:17]
	v_mfma_f32_32x32x16_bf16 v[18:33], v[192:195], v[140:143], v[18:33]
	v_mfma_f32_32x32x16_bf16 v[2:17], v[192:195], v[144:147], v[2:17]
	v_mfma_f32_32x32x16_bf16 v[18:33], v[192:195], v[148:151], v[18:33]
	v_lshlrev_b32_e32 v252, 16, v192
	v_and_b32_e32 v253, 0xffff0000, v192
	v_sub_f32_e32 v62, v54, v252
	v_sub_f32_e32 v63, v55, v253
	v_lshlrev_b32_e32 v252, 16, v193
	v_and_b32_e32 v253, 0xffff0000, v193
	v_sub_f32_e32 v64, v56, v252
	v_sub_f32_e32 v65, v57, v253
	v_lshlrev_b32_e32 v252, 16, v194
	v_and_b32_e32 v253, 0xffff0000, v194
	v_sub_f32_e32 v66, v58, v252
	v_sub_f32_e32 v67, v59, v253
	v_lshlrev_b32_e32 v252, 16, v195
	v_and_b32_e32 v253, 0xffff0000, v195
	v_sub_f32_e32 v68, v60, v252
	v_sub_f32_e32 v69, v61, v253
	v_cvt_pk_bf16_f32 v248, v62, v63
	v_cvt_pk_bf16_f32 v249, v64, v65
	v_cvt_pk_bf16_f32 v250, v66, v67
	v_cvt_pk_bf16_f32 v251, v68, v69
	s_nop 1
	v_mfma_f32_32x32x16_bf16 v[2:17], v[248:251], v[136:139], v[2:17]
	v_mfma_f32_32x32x16_bf16 v[18:33], v[248:251], v[140:143], v[18:33]
	global_load_dwordx4 v[132:135], v[196:197], off offset:416 nt
	global_load_dwordx4 v[136:139], v[34:35], off offset:1024
	global_load_dwordx4 v[140:143], v[36:37], off offset:1024
	global_load_dwordx4 v[144:147], v[38:39], off offset:1024
	global_load_dwordx4 v[148:151], v[40:41], off offset:1024
	s_waitcnt lgkmcnt(0)
	ds_read_b128 v[224:227], v111 offset:704
	ds_read_b128 v[228:231], v111 offset:720
	ds_read_b128 v[232:235], v111 offset:1728
	ds_read_b128 v[236:239], v111 offset:1744
	ds_read_b128 v[240:243], v111 offset:2752
	ds_read_b128 v[244:247], v111 offset:2768
	s_waitcnt vmcnt(18)
	v_lshlrev_b32_e32 v54, 16, v152
	v_and_b32_e32 v55, 0xffff0000, v152
	v_lshlrev_b32_e32 v56, 16, v153
	v_and_b32_e32 v57, 0xffff0000, v153
	v_lshlrev_b32_e32 v58, 16, v154
	v_and_b32_e32 v59, 0xffff0000, v154
	v_lshlrev_b32_e32 v60, 16, v155
	v_and_b32_e32 v61, 0xffff0000, v155
	v_pk_mul_f32 v[54:55], v[46:47], v[54:55]
	v_pk_mul_f32 v[56:57], v[46:47], v[56:57]
	v_pk_mul_f32 v[58:59], v[46:47], v[58:59]
	v_pk_mul_f32 v[60:61], v[46:47], v[60:61]
	v_pk_mul_f32 v[54:55], v[200:201], v[54:55]
	v_pk_mul_f32 v[56:57], v[202:203], v[56:57]
	v_pk_mul_f32 v[58:59], v[204:205], v[58:59]
	v_pk_mul_f32 v[60:61], v[206:207], v[60:61]
	v_pk_fma_f32 v[54:55], v[208:209], v[54:55], v[216:217]
	v_pk_fma_f32 v[56:57], v[210:211], v[56:57], v[218:219]
	v_pk_fma_f32 v[58:59], v[212:213], v[58:59], v[220:221]
	v_pk_fma_f32 v[60:61], v[214:215], v[60:61], v[222:223]
	v_med3_f32 v62, v54, s82, v108
	v_med3_f32 v63, v55, s82, v108
	v_med3_f32 v64, v56, s82, v108
	v_med3_f32 v65, v57, s82, v108
	v_med3_f32 v66, v58, s82, v108
	v_med3_f32 v67, v59, s82, v108
	v_med3_f32 v68, v60, s82, v108
	v_med3_f32 v69, v61, s82, v108
	v_cvt_pk_bf16_f32 v192, v54, v55
	v_cvt_pk_bf16_f32 v193, v56, v57
	v_cvt_pk_bf16_f32 v194, v58, v59
	v_cvt_pk_bf16_f32 v195, v60, v61
	v_cvt_pk_fp8_f32 v70, v62, v63
	v_cvt_pk_fp8_f32 v71, v66, v67
	v_cvt_pk_fp8_f32 v70, v64, v65 op_sel:[0,0,1]
	v_cvt_pk_fp8_f32 v71, v68, v69 op_sel:[0,0,1]
	s_nop 0
	global_store_dwordx2 v[72:73], v[70:71], off offset:160
	v_mfma_f32_32x32x16_bf16 v[2:17], v[192:195], v[156:159], v[2:17]
	v_mfma_f32_32x32x16_bf16 v[18:33], v[192:195], v[160:163], v[18:33]
	v_mfma_f32_32x32x16_bf16 v[2:17], v[192:195], v[164:167], v[2:17]
	v_mfma_f32_32x32x16_bf16 v[18:33], v[192:195], v[168:171], v[18:33]
	v_lshlrev_b32_e32 v252, 16, v192
	v_and_b32_e32 v253, 0xffff0000, v192
	v_sub_f32_e32 v62, v54, v252
	v_sub_f32_e32 v63, v55, v253
	v_lshlrev_b32_e32 v252, 16, v193
	v_and_b32_e32 v253, 0xffff0000, v193
	v_sub_f32_e32 v64, v56, v252
	v_sub_f32_e32 v65, v57, v253
	v_lshlrev_b32_e32 v252, 16, v194
	v_and_b32_e32 v253, 0xffff0000, v194
	v_sub_f32_e32 v66, v58, v252
	v_sub_f32_e32 v67, v59, v253
	v_lshlrev_b32_e32 v252, 16, v195
	v_and_b32_e32 v253, 0xffff0000, v195
	v_sub_f32_e32 v68, v60, v252
	v_sub_f32_e32 v69, v61, v253
	v_cvt_pk_bf16_f32 v248, v62, v63
	v_cvt_pk_bf16_f32 v249, v64, v65
	v_cvt_pk_bf16_f32 v250, v66, v67
	v_cvt_pk_bf16_f32 v251, v68, v69
	s_nop 1
	v_mfma_f32_32x32x16_bf16 v[2:17], v[248:251], v[156:159], v[2:17]
	v_mfma_f32_32x32x16_bf16 v[18:33], v[248:251], v[160:163], v[18:33]
	global_load_dwordx4 v[152:155], v[196:197], off offset:448 nt
	global_load_dwordx4 v[156:159], v[34:35], off offset:2048
	global_load_dwordx4 v[160:163], v[36:37], off offset:2048
	global_load_dwordx4 v[164:167], v[38:39], off offset:2048
	global_load_dwordx4 v[168:171], v[40:41], off offset:2048
	s_waitcnt lgkmcnt(0)
	ds_read_b128 v[200:203], v111 offset:768
	ds_read_b128 v[204:207], v111 offset:784
	ds_read_b128 v[208:211], v111 offset:1792
	ds_read_b128 v[212:215], v111 offset:1808
	ds_read_b128 v[216:219], v111 offset:2816
	ds_read_b128 v[220:223], v111 offset:2832
	s_waitcnt vmcnt(18)
	v_lshlrev_b32_e32 v54, 16, v172
	v_and_b32_e32 v55, 0xffff0000, v172
	v_lshlrev_b32_e32 v56, 16, v173
	v_and_b32_e32 v57, 0xffff0000, v173
	v_lshlrev_b32_e32 v58, 16, v174
	v_and_b32_e32 v59, 0xffff0000, v174
	v_lshlrev_b32_e32 v60, 16, v175
	v_and_b32_e32 v61, 0xffff0000, v175
	v_pk_mul_f32 v[54:55], v[46:47], v[54:55]
	v_pk_mul_f32 v[56:57], v[46:47], v[56:57]
	v_pk_mul_f32 v[58:59], v[46:47], v[58:59]
	v_pk_mul_f32 v[60:61], v[46:47], v[60:61]
	v_pk_mul_f32 v[54:55], v[224:225], v[54:55]
	v_pk_mul_f32 v[56:57], v[226:227], v[56:57]
	v_pk_mul_f32 v[58:59], v[228:229], v[58:59]
	v_pk_mul_f32 v[60:61], v[230:231], v[60:61]
	v_pk_fma_f32 v[54:55], v[232:233], v[54:55], v[240:241]
	v_pk_fma_f32 v[56:57], v[234:235], v[56:57], v[242:243]
	v_pk_fma_f32 v[58:59], v[236:237], v[58:59], v[244:245]
	v_pk_fma_f32 v[60:61], v[238:239], v[60:61], v[246:247]
	v_med3_f32 v62, v54, s82, v108
	v_med3_f32 v63, v55, s82, v108
	v_med3_f32 v64, v56, s82, v108
	v_med3_f32 v65, v57, s82, v108
	v_med3_f32 v66, v58, s82, v108
	v_med3_f32 v67, v59, s82, v108
	v_med3_f32 v68, v60, s82, v108
	v_med3_f32 v69, v61, s82, v108
	v_cvt_pk_bf16_f32 v192, v54, v55
	v_cvt_pk_bf16_f32 v193, v56, v57
	v_cvt_pk_bf16_f32 v194, v58, v59
	v_cvt_pk_bf16_f32 v195, v60, v61
	v_cvt_pk_fp8_f32 v70, v62, v63
	v_cvt_pk_fp8_f32 v71, v66, v67
	v_cvt_pk_fp8_f32 v70, v64, v65 op_sel:[0,0,1]
	v_cvt_pk_fp8_f32 v71, v68, v69 op_sel:[0,0,1]
	s_nop 0
	global_store_dwordx2 v[72:73], v[70:71], off offset:176
	v_mfma_f32_32x32x16_bf16 v[2:17], v[192:195], v[176:179], v[2:17]
	v_mfma_f32_32x32x16_bf16 v[18:33], v[192:195], v[180:183], v[18:33]
	v_mfma_f32_32x32x16_bf16 v[2:17], v[192:195], v[184:187], v[2:17]
	v_mfma_f32_32x32x16_bf16 v[18:33], v[192:195], v[188:191], v[18:33]
	v_lshlrev_b32_e32 v252, 16, v192
	v_and_b32_e32 v253, 0xffff0000, v192
	v_sub_f32_e32 v62, v54, v252
	v_sub_f32_e32 v63, v55, v253
	v_lshlrev_b32_e32 v252, 16, v193
	v_and_b32_e32 v253, 0xffff0000, v193
	v_sub_f32_e32 v64, v56, v252
	v_sub_f32_e32 v65, v57, v253
	v_lshlrev_b32_e32 v252, 16, v194
	v_and_b32_e32 v253, 0xffff0000, v194
	v_sub_f32_e32 v66, v58, v252
	v_sub_f32_e32 v67, v59, v253
	v_lshlrev_b32_e32 v252, 16, v195
	v_and_b32_e32 v253, 0xffff0000, v195
	v_sub_f32_e32 v68, v60, v252
	v_sub_f32_e32 v69, v61, v253
	v_cvt_pk_bf16_f32 v248, v62, v63
	v_cvt_pk_bf16_f32 v249, v64, v65
	v_cvt_pk_bf16_f32 v250, v66, v67
	v_cvt_pk_bf16_f32 v251, v68, v69
	s_nop 1
	v_mfma_f32_32x32x16_bf16 v[2:17], v[248:251], v[176:179], v[2:17]
	v_mfma_f32_32x32x16_bf16 v[18:33], v[248:251], v[180:183], v[18:33]
	global_load_dwordx4 v[172:175], v[196:197], off offset:480 nt
	global_load_dwordx4 v[176:179], v[34:35], off offset:3072
	global_load_dwordx4 v[180:183], v[36:37], off offset:3072
	global_load_dwordx4 v[184:187], v[38:39], off offset:3072
	global_load_dwordx4 v[188:191], v[40:41], off offset:3072
	s_waitcnt lgkmcnt(0)
	ds_read_b128 v[224:227], v111 offset:832
	ds_read_b128 v[228:231], v111 offset:848
	ds_read_b128 v[232:235], v111 offset:1856
	ds_read_b128 v[236:239], v111 offset:1872
	ds_read_b128 v[240:243], v111 offset:2880
	ds_read_b128 v[244:247], v111 offset:2896
	s_waitcnt vmcnt(18)
	v_lshlrev_b32_e32 v54, 16, v112
	v_and_b32_e32 v55, 0xffff0000, v112
	v_lshlrev_b32_e32 v56, 16, v113
	v_and_b32_e32 v57, 0xffff0000, v113
	v_lshlrev_b32_e32 v58, 16, v114
	v_and_b32_e32 v59, 0xffff0000, v114
	v_lshlrev_b32_e32 v60, 16, v115
	v_and_b32_e32 v61, 0xffff0000, v115
	v_pk_mul_f32 v[54:55], v[46:47], v[54:55]
	v_pk_mul_f32 v[56:57], v[46:47], v[56:57]
	v_pk_mul_f32 v[58:59], v[46:47], v[58:59]
	v_pk_mul_f32 v[60:61], v[46:47], v[60:61]
	v_pk_mul_f32 v[54:55], v[200:201], v[54:55]
	v_pk_mul_f32 v[56:57], v[202:203], v[56:57]
	v_pk_mul_f32 v[58:59], v[204:205], v[58:59]
	v_pk_mul_f32 v[60:61], v[206:207], v[60:61]
	v_pk_fma_f32 v[54:55], v[208:209], v[54:55], v[216:217]
	v_pk_fma_f32 v[56:57], v[210:211], v[56:57], v[218:219]
	v_pk_fma_f32 v[58:59], v[212:213], v[58:59], v[220:221]
	v_pk_fma_f32 v[60:61], v[214:215], v[60:61], v[222:223]
	v_med3_f32 v62, v54, s82, v108
	v_med3_f32 v63, v55, s82, v108
	v_med3_f32 v64, v56, s82, v108
	v_med3_f32 v65, v57, s82, v108
	v_med3_f32 v66, v58, s82, v108
	v_med3_f32 v67, v59, s82, v108
	v_med3_f32 v68, v60, s82, v108
	v_med3_f32 v69, v61, s82, v108
	v_cvt_pk_bf16_f32 v192, v54, v55
	v_cvt_pk_bf16_f32 v193, v56, v57
	v_cvt_pk_bf16_f32 v194, v58, v59
	v_cvt_pk_bf16_f32 v195, v60, v61
	v_cvt_pk_fp8_f32 v70, v62, v63
	v_cvt_pk_fp8_f32 v71, v66, v67
	v_cvt_pk_fp8_f32 v70, v64, v65 op_sel:[0,0,1]
	v_cvt_pk_fp8_f32 v71, v68, v69 op_sel:[0,0,1]
	s_nop 0
	global_store_dwordx2 v[72:73], v[70:71], off offset:192
	v_mfma_f32_32x32x16_bf16 v[2:17], v[192:195], v[116:119], v[2:17]
	v_mfma_f32_32x32x16_bf16 v[18:33], v[192:195], v[120:123], v[18:33]
	v_mfma_f32_32x32x16_bf16 v[2:17], v[192:195], v[124:127], v[2:17]
	v_mfma_f32_32x32x16_bf16 v[18:33], v[192:195], v[128:131], v[18:33]
	v_lshlrev_b32_e32 v252, 16, v192
	v_and_b32_e32 v253, 0xffff0000, v192
	v_sub_f32_e32 v62, v54, v252
	v_sub_f32_e32 v63, v55, v253
	v_lshlrev_b32_e32 v252, 16, v193
	v_and_b32_e32 v253, 0xffff0000, v193
	v_sub_f32_e32 v64, v56, v252
	v_sub_f32_e32 v65, v57, v253
	v_lshlrev_b32_e32 v252, 16, v194
	v_and_b32_e32 v253, 0xffff0000, v194
	v_sub_f32_e32 v66, v58, v252
	v_sub_f32_e32 v67, v59, v253
	v_lshlrev_b32_e32 v252, 16, v195
	v_and_b32_e32 v253, 0xffff0000, v195
	v_sub_f32_e32 v68, v60, v252
	v_sub_f32_e32 v69, v61, v253
	v_cvt_pk_bf16_f32 v248, v62, v63
	v_cvt_pk_bf16_f32 v249, v64, v65
	v_cvt_pk_bf16_f32 v250, v66, v67
	v_cvt_pk_bf16_f32 v251, v68, v69
	s_nop 1
	v_mfma_f32_32x32x16_bf16 v[2:17], v[248:251], v[116:119], v[2:17]
	v_mfma_f32_32x32x16_bf16 v[18:33], v[248:251], v[120:123], v[18:33]
	s_waitcnt lgkmcnt(0)
	ds_read_b128 v[200:203], v111 offset:896
	ds_read_b128 v[204:207], v111 offset:912
	ds_read_b128 v[208:211], v111 offset:1920
	ds_read_b128 v[212:215], v111 offset:1936
	ds_read_b128 v[216:219], v111 offset:2944
	ds_read_b128 v[220:223], v111 offset:2960
	s_waitcnt vmcnt(13)
	v_lshlrev_b32_e32 v54, 16, v132
	v_and_b32_e32 v55, 0xffff0000, v132
	v_lshlrev_b32_e32 v56, 16, v133
	v_and_b32_e32 v57, 0xffff0000, v133
	v_lshlrev_b32_e32 v58, 16, v134
	v_and_b32_e32 v59, 0xffff0000, v134
	v_lshlrev_b32_e32 v60, 16, v135
	v_and_b32_e32 v61, 0xffff0000, v135
	v_pk_mul_f32 v[54:55], v[46:47], v[54:55]
	v_pk_mul_f32 v[56:57], v[46:47], v[56:57]
	v_pk_mul_f32 v[58:59], v[46:47], v[58:59]
	v_pk_mul_f32 v[60:61], v[46:47], v[60:61]
	v_pk_mul_f32 v[54:55], v[224:225], v[54:55]
	v_pk_mul_f32 v[56:57], v[226:227], v[56:57]
	v_pk_mul_f32 v[58:59], v[228:229], v[58:59]
	v_pk_mul_f32 v[60:61], v[230:231], v[60:61]
	v_pk_fma_f32 v[54:55], v[232:233], v[54:55], v[240:241]
	v_pk_fma_f32 v[56:57], v[234:235], v[56:57], v[242:243]
	v_pk_fma_f32 v[58:59], v[236:237], v[58:59], v[244:245]
	v_pk_fma_f32 v[60:61], v[238:239], v[60:61], v[246:247]
	v_med3_f32 v62, v54, s82, v108
	v_med3_f32 v63, v55, s82, v108
	v_med3_f32 v64, v56, s82, v108
	v_med3_f32 v65, v57, s82, v108
	v_med3_f32 v66, v58, s82, v108
	v_med3_f32 v67, v59, s82, v108
	v_med3_f32 v68, v60, s82, v108
	v_med3_f32 v69, v61, s82, v108
	v_cvt_pk_bf16_f32 v192, v54, v55
	v_cvt_pk_bf16_f32 v193, v56, v57
	v_cvt_pk_bf16_f32 v194, v58, v59
	v_cvt_pk_bf16_f32 v195, v60, v61
	v_cvt_pk_fp8_f32 v70, v62, v63
	v_cvt_pk_fp8_f32 v71, v66, v67
	v_cvt_pk_fp8_f32 v70, v64, v65 op_sel:[0,0,1]
	v_cvt_pk_fp8_f32 v71, v68, v69 op_sel:[0,0,1]
	s_nop 0
	global_store_dwordx2 v[72:73], v[70:71], off offset:208
	v_mfma_f32_32x32x16_bf16 v[2:17], v[192:195], v[136:139], v[2:17]
	v_mfma_f32_32x32x16_bf16 v[18:33], v[192:195], v[140:143], v[18:33]
	v_mfma_f32_32x32x16_bf16 v[2:17], v[192:195], v[144:147], v[2:17]
	v_mfma_f32_32x32x16_bf16 v[18:33], v[192:195], v[148:151], v[18:33]
	v_lshlrev_b32_e32 v252, 16, v192
	v_and_b32_e32 v253, 0xffff0000, v192
	v_sub_f32_e32 v62, v54, v252
	v_sub_f32_e32 v63, v55, v253
	v_lshlrev_b32_e32 v252, 16, v193
	v_and_b32_e32 v253, 0xffff0000, v193
	v_sub_f32_e32 v64, v56, v252
	v_sub_f32_e32 v65, v57, v253
	v_lshlrev_b32_e32 v252, 16, v194
	v_and_b32_e32 v253, 0xffff0000, v194
	v_sub_f32_e32 v66, v58, v252
	v_sub_f32_e32 v67, v59, v253
	v_lshlrev_b32_e32 v252, 16, v195
	v_and_b32_e32 v253, 0xffff0000, v195
	v_sub_f32_e32 v68, v60, v252
	v_sub_f32_e32 v69, v61, v253
	v_cvt_pk_bf16_f32 v248, v62, v63
	v_cvt_pk_bf16_f32 v249, v64, v65
	v_cvt_pk_bf16_f32 v250, v66, v67
	v_cvt_pk_bf16_f32 v251, v68, v69
	s_nop 1
	v_mfma_f32_32x32x16_bf16 v[2:17], v[248:251], v[136:139], v[2:17]
	v_mfma_f32_32x32x16_bf16 v[18:33], v[248:251], v[140:143], v[18:33]
	s_waitcnt lgkmcnt(0)
	ds_read_b128 v[224:227], v111 offset:960
	ds_read_b128 v[228:231], v111 offset:976
	ds_read_b128 v[232:235], v111 offset:1984
	ds_read_b128 v[236:239], v111 offset:2000
	ds_read_b128 v[240:243], v111 offset:3008
	ds_read_b128 v[244:247], v111 offset:3024
	s_waitcnt vmcnt(8)
	v_lshlrev_b32_e32 v54, 16, v152
	v_and_b32_e32 v55, 0xffff0000, v152
	v_lshlrev_b32_e32 v56, 16, v153
	v_and_b32_e32 v57, 0xffff0000, v153
	v_lshlrev_b32_e32 v58, 16, v154
	v_and_b32_e32 v59, 0xffff0000, v154
	v_lshlrev_b32_e32 v60, 16, v155
	v_and_b32_e32 v61, 0xffff0000, v155
	v_pk_mul_f32 v[54:55], v[46:47], v[54:55]
	v_pk_mul_f32 v[56:57], v[46:47], v[56:57]
	v_pk_mul_f32 v[58:59], v[46:47], v[58:59]
	v_pk_mul_f32 v[60:61], v[46:47], v[60:61]
	v_pk_mul_f32 v[54:55], v[200:201], v[54:55]
	v_pk_mul_f32 v[56:57], v[202:203], v[56:57]
	v_pk_mul_f32 v[58:59], v[204:205], v[58:59]
	v_pk_mul_f32 v[60:61], v[206:207], v[60:61]
	v_pk_fma_f32 v[54:55], v[208:209], v[54:55], v[216:217]
	v_pk_fma_f32 v[56:57], v[210:211], v[56:57], v[218:219]
	v_pk_fma_f32 v[58:59], v[212:213], v[58:59], v[220:221]
	v_pk_fma_f32 v[60:61], v[214:215], v[60:61], v[222:223]
	v_med3_f32 v62, v54, s82, v108
	v_med3_f32 v63, v55, s82, v108
	v_med3_f32 v64, v56, s82, v108
	v_med3_f32 v65, v57, s82, v108
	v_med3_f32 v66, v58, s82, v108
	v_med3_f32 v67, v59, s82, v108
	v_med3_f32 v68, v60, s82, v108
	v_med3_f32 v69, v61, s82, v108
	v_cvt_pk_bf16_f32 v192, v54, v55
	v_cvt_pk_bf16_f32 v193, v56, v57
	v_cvt_pk_bf16_f32 v194, v58, v59
	v_cvt_pk_bf16_f32 v195, v60, v61
	v_cvt_pk_fp8_f32 v70, v62, v63
	v_cvt_pk_fp8_f32 v71, v66, v67
	v_cvt_pk_fp8_f32 v70, v64, v65 op_sel:[0,0,1]
	v_cvt_pk_fp8_f32 v71, v68, v69 op_sel:[0,0,1]
	s_nop 0
	global_store_dwordx2 v[72:73], v[70:71], off offset:224
	v_mfma_f32_32x32x16_bf16 v[2:17], v[192:195], v[156:159], v[2:17]
	v_mfma_f32_32x32x16_bf16 v[18:33], v[192:195], v[160:163], v[18:33]
	v_mfma_f32_32x32x16_bf16 v[2:17], v[192:195], v[164:167], v[2:17]
	v_mfma_f32_32x32x16_bf16 v[18:33], v[192:195], v[168:171], v[18:33]
	v_lshlrev_b32_e32 v252, 16, v192
	v_and_b32_e32 v253, 0xffff0000, v192
	v_sub_f32_e32 v62, v54, v252
	v_sub_f32_e32 v63, v55, v253
	v_lshlrev_b32_e32 v252, 16, v193
	v_and_b32_e32 v253, 0xffff0000, v193
	v_sub_f32_e32 v64, v56, v252
	v_sub_f32_e32 v65, v57, v253
	v_lshlrev_b32_e32 v252, 16, v194
	v_and_b32_e32 v253, 0xffff0000, v194
	v_sub_f32_e32 v66, v58, v252
	v_sub_f32_e32 v67, v59, v253
	v_lshlrev_b32_e32 v252, 16, v195
	v_and_b32_e32 v253, 0xffff0000, v195
	v_sub_f32_e32 v68, v60, v252
	v_sub_f32_e32 v69, v61, v253
	v_cvt_pk_bf16_f32 v248, v62, v63
	v_cvt_pk_bf16_f32 v249, v64, v65
	v_cvt_pk_bf16_f32 v250, v66, v67
	v_cvt_pk_bf16_f32 v251, v68, v69
	s_nop 1
	v_mfma_f32_32x32x16_bf16 v[2:17], v[248:251], v[156:159], v[2:17]
	v_mfma_f32_32x32x16_bf16 v[18:33], v[248:251], v[160:163], v[18:33]
	s_waitcnt lgkmcnt(0)
	s_waitcnt vmcnt(3)
	v_lshlrev_b32_e32 v54, 16, v172
	v_and_b32_e32 v55, 0xffff0000, v172
	v_lshlrev_b32_e32 v56, 16, v173
	v_and_b32_e32 v57, 0xffff0000, v173
	v_lshlrev_b32_e32 v58, 16, v174
	v_and_b32_e32 v59, 0xffff0000, v174
	v_lshlrev_b32_e32 v60, 16, v175
	v_and_b32_e32 v61, 0xffff0000, v175
	v_pk_mul_f32 v[54:55], v[46:47], v[54:55]
	v_pk_mul_f32 v[56:57], v[46:47], v[56:57]
	v_pk_mul_f32 v[58:59], v[46:47], v[58:59]
	v_pk_mul_f32 v[60:61], v[46:47], v[60:61]
	v_pk_mul_f32 v[54:55], v[224:225], v[54:55]
	v_pk_mul_f32 v[56:57], v[226:227], v[56:57]
	v_pk_mul_f32 v[58:59], v[228:229], v[58:59]
	v_pk_mul_f32 v[60:61], v[230:231], v[60:61]
	v_pk_fma_f32 v[54:55], v[232:233], v[54:55], v[240:241]
	v_pk_fma_f32 v[56:57], v[234:235], v[56:57], v[242:243]
	v_pk_fma_f32 v[58:59], v[236:237], v[58:59], v[244:245]
	v_pk_fma_f32 v[60:61], v[238:239], v[60:61], v[246:247]
	v_med3_f32 v62, v54, s82, v108
	v_med3_f32 v63, v55, s82, v108
	v_med3_f32 v64, v56, s82, v108
	v_med3_f32 v65, v57, s82, v108
	v_med3_f32 v66, v58, s82, v108
	v_med3_f32 v67, v59, s82, v108
	v_med3_f32 v68, v60, s82, v108
	v_med3_f32 v69, v61, s82, v108
	v_cvt_pk_bf16_f32 v192, v54, v55
	v_cvt_pk_bf16_f32 v193, v56, v57
	v_cvt_pk_bf16_f32 v194, v58, v59
	v_cvt_pk_bf16_f32 v195, v60, v61
	v_cvt_pk_fp8_f32 v70, v62, v63
	v_cvt_pk_fp8_f32 v71, v66, v67
	v_cvt_pk_fp8_f32 v70, v64, v65 op_sel:[0,0,1]
	v_cvt_pk_fp8_f32 v71, v68, v69 op_sel:[0,0,1]
	s_nop 0
	global_store_dwordx2 v[72:73], v[70:71], off offset:240
	v_mfma_f32_32x32x16_bf16 v[2:17], v[192:195], v[176:179], v[2:17]
	v_mfma_f32_32x32x16_bf16 v[18:33], v[192:195], v[180:183], v[18:33]
	v_mfma_f32_32x32x16_bf16 v[2:17], v[192:195], v[184:187], v[2:17]
	v_mfma_f32_32x32x16_bf16 v[18:33], v[192:195], v[188:191], v[18:33]
	v_lshlrev_b32_e32 v252, 16, v192
	v_and_b32_e32 v253, 0xffff0000, v192
	v_sub_f32_e32 v62, v54, v252
	v_sub_f32_e32 v63, v55, v253
	v_lshlrev_b32_e32 v252, 16, v193
	v_and_b32_e32 v253, 0xffff0000, v193
	v_sub_f32_e32 v64, v56, v252
	v_sub_f32_e32 v65, v57, v253
	v_lshlrev_b32_e32 v252, 16, v194
	v_and_b32_e32 v253, 0xffff0000, v194
	v_sub_f32_e32 v66, v58, v252
	v_sub_f32_e32 v67, v59, v253
	v_lshlrev_b32_e32 v252, 16, v195
	v_and_b32_e32 v253, 0xffff0000, v195
	v_sub_f32_e32 v68, v60, v252
	v_sub_f32_e32 v69, v61, v253
	v_cvt_pk_bf16_f32 v248, v62, v63
	v_cvt_pk_bf16_f32 v249, v64, v65
	v_cvt_pk_bf16_f32 v250, v66, v67
	v_cvt_pk_bf16_f32 v251, v68, v69
	s_nop 1
	v_mfma_f32_32x32x16_bf16 v[2:17], v[248:251], v[176:179], v[2:17]
	v_mfma_f32_32x32x16_bf16 v[18:33], v[248:251], v[180:183], v[18:33]
	v_and_b32_e32 v62, 0xffffff00, v103
	v_lshlrev_b32_e32 v62, 6, v62
	v_lshl_add_u32 v62, v254, 4, v62
	v_lshlrev_b32_e32 v63, 12, v75
	v_sub_u32_e32 v62, v62, v63
	v_add_u32_e32 v62, 0x3000, v62
	v_sub_u32_e32 v62, 0, v62
	v_ashrrev_i32_e32 v63, 31, v62
	v_lshl_add_u64 v[34:35], v[34:35], 0, v[62:63]
	v_lshl_add_u64 v[36:37], v[36:37], 0, v[62:63]
	v_lshl_add_u64 v[38:39], v[38:39], 0, v[62:63]
	v_lshl_add_u64 v[40:41], v[40:41], 0, v[62:63]
	s_nop 7
	v_add_u32_e32 v1, 0x400, v83
	s_nop 9
	ds_write2_b32 v1, v2, v18 offset1:32
	ds_write2_b32 v1, v3, v19 offset0:64 offset1:96
	ds_write2_b32 v1, v4, v20 offset0:128 offset1:160
	ds_write2_b32 v1, v5, v21 offset0:192 offset1:224
	v_add_u32_e32 v1, 0xc00, v83
	ds_write2_b32 v1, v6, v22 offset1:32
	ds_write2_b32 v1, v7, v23 offset0:64 offset1:96
	ds_write2_b32 v1, v8, v24 offset0:128 offset1:160
	ds_write2_b32 v1, v9, v25 offset0:192 offset1:224
	v_add_u32_e32 v1, 0x1400, v83
	ds_write2_b32 v1, v10, v26 offset1:32
	ds_write2_b32 v1, v11, v27 offset0:64 offset1:96
	ds_write2_b32 v1, v12, v28 offset0:128 offset1:160
	ds_write2_b32 v1, v13, v29 offset0:192 offset1:224
	v_add_u32_e32 v1, 0x1c00, v83
	ds_write2_b32 v1, v14, v30 offset1:32
	ds_write2_b32 v1, v15, v31 offset0:64 offset1:96
	ds_write2_b32 v1, v16, v32 offset0:128 offset1:160
	ds_write2_b32 v1, v17, v33 offset0:192 offset1:224
	s_waitcnt lgkmcnt(0)
	s_barrier
	global_load_dword v1, v[42:43], off
	v_add_u32_e32 v8, s66, v84
	ds_read2st64_b32 v[2:3], v8 offset0:4 offset1:36
	ds_read2st64_b32 v[4:5], v8 offset0:68 offset1:100
	ds_read2st64_b32 v[6:7], v8 offset0:132 offset1:164
	ds_read2st64_b32 v[8:9], v8 offset0:196 offset1:228
	s_waitcnt lgkmcnt(3)
	v_add_f32_e32 v2, 0, v2
	v_add_f32_e32 v2, v2, v3
	s_waitcnt lgkmcnt(2)
	v_add_f32_e32 v2, v2, v4
	v_add_f32_e32 v2, v2, v5
	s_waitcnt lgkmcnt(1)
	v_add_f32_e32 v2, v2, v6
	v_add_f32_e32 v2, v2, v7
	s_waitcnt lgkmcnt(0)
	v_add_f32_e32 v2, v2, v8
	v_add_f32_e32 v2, v2, v9
	v_mul_f32_e32 v3, 0xbfb8aa3b, v2
	v_fma_f32 v4, v2, s83, -v3
	v_rndne_f32_e32 v5, v3
	v_fmac_f32_e32 v4, 0xb2a5705f, v2
	v_sub_f32_e32 v3, v3, v5
	v_add_f32_e32 v3, v3, v4
	v_cvt_i32_f32_e32 v5, v5
	v_exp_f32_e32 v3, v3
	v_cmp_nlt_f32_e32 vcc, s84, v2
	v_ldexp_f32 v3, v3, v5
	s_nop 0
	v_cndmask_b32_e32 v3, 0, v3, vcc
	v_cmp_ngt_f32_e32 vcc, s85, v2
	s_nop 1
	v_cndmask_b32_e32 v2, v109, v3, vcc
	v_add_f32_e32 v2, 1.0, v2
	v_div_scale_f32 v3, s[34:35], v2, v2, 1.0
	v_rcp_f32_e32 v4, v3
	v_div_scale_f32 v5, vcc, 1.0, v2, 1.0
	v_fma_f32 v6, -v3, v4, 1.0
	v_fmac_f32_e32 v4, v6, v4
	v_mul_f32_e32 v6, v5, v4
	v_fma_f32 v7, -v3, v6, v5
	v_fmac_f32_e32 v6, v7, v4
	v_fma_f32 v3, -v3, v6, v5
	v_div_fmas_f32 v3, v3, v4, v6
	v_div_fixup_f32 v2, v3, v2, 1.0
	s_waitcnt vmcnt(0)
	v_mov_b32_e32 v128, v1
	v_add_f32_e32 v1, v1, v2
	ds_bpermute_b32 v3, v88, v1
	ds_bpermute_b32 v4, v89, v1
	ds_bpermute_b32 v5, v90, v1
	ds_bpermute_b32 v6, v91, v1
	ds_bpermute_b32 v7, v92, v1
	s_waitcnt lgkmcnt(4)
	v_cmp_eq_f32_e64 s[34:35], v1, v3
	v_cmp_lt_f32_e32 vcc, v1, v3
	s_waitcnt lgkmcnt(3)
	v_cmp_eq_f32_e64 s[38:39], v1, v4
	s_and_b64 s[34:35], s[4:5], s[34:35]
	v_cmp_lt_f32_e64 s[36:37], v1, v4
	s_waitcnt lgkmcnt(2)
	v_cmp_eq_f32_e64 s[42:43], v1, v5
	s_and_b64 s[38:39], s[6:7], s[38:39]
	s_or_b64 s[34:35], vcc, s[34:35]
	v_cmp_lt_f32_e64 s[40:41], v1, v5
	s_waitcnt lgkmcnt(1)
	v_cmp_eq_f32_e64 s[46:47], v1, v6
	s_and_b64 s[42:43], s[8:9], s[42:43]
	v_cndmask_b32_e64 v3, 0, 1, s[34:35]
	s_or_b64 s[34:35], s[36:37], s[38:39]
	v_cmp_lt_f32_e64 s[44:45], v1, v6
	s_and_b64 s[46:47], s[10:11], s[46:47]
	v_cndmask_b32_e64 v4, 0, 1, s[34:35]
	s_or_b64 s[34:35], s[40:41], s[42:43]
	v_cndmask_b32_e64 v5, 0, 1, s[34:35]
	s_or_b64 s[34:35], s[44:45], s[46:47]
	v_add3_u32 v3, v3, v4, v5
	v_cndmask_b32_e64 v4, 0, 1, s[34:35]
	s_waitcnt lgkmcnt(0)
	v_cmp_eq_f32_e64 s[34:35], v1, v7
	v_cmp_lt_f32_e32 vcc, v1, v7
	ds_bpermute_b32 v5, v93, v1
	s_and_b64 s[34:35], s[12:13], s[34:35]
	s_or_b64 s[34:35], vcc, s[34:35]
	v_cndmask_b32_e64 v6, 0, 1, s[34:35]
	v_add3_u32 v3, v3, v4, v6
	ds_bpermute_b32 v4, v94, v1
	s_waitcnt lgkmcnt(1)
	v_cmp_eq_f32_e64 s[34:35], v1, v5
	ds_bpermute_b32 v6, v95, v1
	v_cmp_lt_f32_e32 vcc, v1, v5
	s_and_b64 s[34:35], s[14:15], s[34:35]
	s_or_b64 s[34:35], vcc, s[34:35]
	v_cndmask_b32_e64 v5, 0, 1, s[34:35]
	s_waitcnt lgkmcnt(1)
	v_cmp_eq_f32_e64 s[34:35], v1, v4
	v_cmp_lt_f32_e32 vcc, v1, v4
	s_and_b64 s[34:35], s[16:17], s[34:35]
	s_or_b64 s[34:35], vcc, s[34:35]
	s_waitcnt lgkmcnt(0)
	v_cmp_lt_f32_e32 vcc, v1, v6
	v_cndmask_b32_e64 v4, 0, 1, s[34:35]
	s_mov_b32 s40, 0
	v_addc_co_u32_e32 v3, vcc, v3, v5, vcc
	v_add_u32_e32 v3, v3, v4
	v_cmp_gt_u32_e32 vcc, 2, v3
	s_nop 1
	v_cndmask_b32_e32 v3, 0, v1, vcc
	ds_bpermute_b32 v4, v76, v3
	s_waitcnt lgkmcnt(0)
	v_add_f32_e32 v3, v3, v4
	ds_bpermute_b32 v4, v77, v3
	s_waitcnt lgkmcnt(0)
	v_add_f32_e32 v3, v3, v4
	ds_bpermute_b32 v4, v78, v3
	s_waitcnt lgkmcnt(0)
	v_add_f32_e32 v3, v3, v4
	ds_bpermute_b32 v4, v87, v3
	ds_bpermute_b32 v5, v96, v3
	ds_bpermute_b32 v6, v97, v3
	ds_bpermute_b32 v7, v98, v3
	ds_bpermute_b32 v8, v99, v3
	s_waitcnt lgkmcnt(4)
	v_cmp_eq_f32_e64 s[34:35], v3, v4
	v_cmp_lt_f32_e32 vcc, v3, v4
	s_and_b64 s[34:35], s[18:19], s[34:35]
	s_or_b64 s[34:35], vcc, s[34:35]
	v_cndmask_b32_e64 v4, 0, 1, s[34:35]
	s_waitcnt lgkmcnt(3)
	v_cmp_eq_f32_e64 s[34:35], v3, v5
	v_cmp_lt_f32_e32 vcc, v3, v5
	s_and_b64 s[34:35], s[20:21], s[34:35]
	s_or_b64 s[34:35], vcc, s[34:35]
	v_cndmask_b32_e64 v5, 0, 1, s[34:35]
	s_waitcnt lgkmcnt(2)
	v_cmp_eq_f32_e64 s[34:35], v3, v6
	v_cmp_lt_f32_e32 vcc, v3, v6
	s_and_b64 s[34:35], s[22:23], s[34:35]
	s_or_b64 s[34:35], vcc, s[34:35]
	v_cndmask_b32_e64 v6, 0, 1, s[34:35]
	s_waitcnt lgkmcnt(1)
	v_cmp_eq_f32_e64 s[34:35], v3, v7
	v_cmp_lt_f32_e32 vcc, v3, v7
	s_and_b64 s[34:35], s[24:25], s[34:35]
	ds_bpermute_b32 v9, v100, v3
	s_or_b64 s[34:35], vcc, s[34:35]
	v_cndmask_b32_e64 v7, 0, 1, s[34:35]
	s_waitcnt lgkmcnt(1)
	v_cmp_eq_f32_e64 s[34:35], v3, v8
	v_cmp_lt_f32_e32 vcc, v3, v8
	s_and_b64 s[34:35], s[26:27], s[34:35]
	ds_bpermute_b32 v10, v101, v3
	s_or_b64 s[34:35], vcc, s[34:35]
	v_cndmask_b32_e64 v8, 0, 1, s[34:35]
	s_waitcnt lgkmcnt(1)
	v_cmp_eq_f32_e64 s[34:35], v3, v9
	ds_bpermute_b32 v11, v102, v3
	v_cmp_lt_f32_e32 vcc, v3, v9
	s_and_b64 s[34:35], s[28:29], s[34:35]
	s_or_b64 s[34:35], vcc, s[34:35]
	v_cndmask_b32_e64 v9, 0, 1, s[34:35]
	s_waitcnt lgkmcnt(1)
	v_cmp_eq_f32_e64 s[34:35], v3, v10
	v_cmp_lt_f32_e32 vcc, v3, v10
	s_and_b64 s[34:35], s[30:31], s[34:35]
	s_or_b64 s[34:35], vcc, s[34:35]
	s_waitcnt lgkmcnt(0)
	v_cmp_lt_f32_e32 vcc, v3, v11
	v_cndmask_b32_e64 v10, 0, 1, s[34:35]
	s_nop 0
	v_cndmask_b32_e64 v3, 0, 1, vcc
	v_add_u32_e32 v3, v5, v3
	v_add3_u32 v3, v3, v4, v6
	v_add3_u32 v3, v3, v7, v8
	v_add3_u32 v3, v3, v9, v10
	v_cmp_gt_u32_e32 vcc, 4, v3
	v_mov_b32_e32 v5, 0
	v_mov_b32_e32 v4, v104
	v_cndmask_b32_e32 v3, v110, v1, vcc
